# phase 0: silu(c) staging loop unrolled with all 32 loads in flight (was one load per round trip); attention items all via second call site
# baseline (speedup 1.0000x reference)
.LBB0_18:
	v_mov_b32_e32 v132, v2
	v_mov_b32_e32 v133, v3
	global_load_dword v100, v[132:133], off
	v_lshl_add_u64 v[132:133], v[132:133], 0, s[6:7]
	global_load_dword v101, v[132:133], off
	v_lshl_add_u64 v[132:133], v[132:133], 0, s[6:7]
	global_load_dword v102, v[132:133], off
	v_lshl_add_u64 v[132:133], v[132:133], 0, s[6:7]
	global_load_dword v103, v[132:133], off
	v_lshl_add_u64 v[132:133], v[132:133], 0, s[6:7]
	global_load_dword v104, v[132:133], off
	v_lshl_add_u64 v[132:133], v[132:133], 0, s[6:7]
	global_load_dword v105, v[132:133], off
	v_lshl_add_u64 v[132:133], v[132:133], 0, s[6:7]
	global_load_dword v106, v[132:133], off
	v_lshl_add_u64 v[132:133], v[132:133], 0, s[6:7]
	global_load_dword v107, v[132:133], off
	v_lshl_add_u64 v[132:133], v[132:133], 0, s[6:7]
	global_load_dword v108, v[132:133], off
	v_lshl_add_u64 v[132:133], v[132:133], 0, s[6:7]
	global_load_dword v109, v[132:133], off
	v_lshl_add_u64 v[132:133], v[132:133], 0, s[6:7]
	global_load_dword v110, v[132:133], off
	v_lshl_add_u64 v[132:133], v[132:133], 0, s[6:7]
	global_load_dword v111, v[132:133], off
	v_lshl_add_u64 v[132:133], v[132:133], 0, s[6:7]
	global_load_dword v112, v[132:133], off
	v_lshl_add_u64 v[132:133], v[132:133], 0, s[6:7]
	global_load_dword v113, v[132:133], off
	v_lshl_add_u64 v[132:133], v[132:133], 0, s[6:7]
	global_load_dword v114, v[132:133], off
	v_lshl_add_u64 v[132:133], v[132:133], 0, s[6:7]
	global_load_dword v115, v[132:133], off
	v_lshl_add_u64 v[132:133], v[132:133], 0, s[6:7]
	global_load_dword v116, v[132:133], off
	v_lshl_add_u64 v[132:133], v[132:133], 0, s[6:7]
	global_load_dword v117, v[132:133], off
	v_lshl_add_u64 v[132:133], v[132:133], 0, s[6:7]
	global_load_dword v118, v[132:133], off
	v_lshl_add_u64 v[132:133], v[132:133], 0, s[6:7]
	global_load_dword v119, v[132:133], off
	v_lshl_add_u64 v[132:133], v[132:133], 0, s[6:7]
	global_load_dword v120, v[132:133], off
	v_lshl_add_u64 v[132:133], v[132:133], 0, s[6:7]
	global_load_dword v121, v[132:133], off
	v_lshl_add_u64 v[132:133], v[132:133], 0, s[6:7]
	global_load_dword v122, v[132:133], off
	v_lshl_add_u64 v[132:133], v[132:133], 0, s[6:7]
	global_load_dword v123, v[132:133], off
	v_lshl_add_u64 v[132:133], v[132:133], 0, s[6:7]
	global_load_dword v124, v[132:133], off
	v_lshl_add_u64 v[132:133], v[132:133], 0, s[6:7]
	global_load_dword v125, v[132:133], off
	v_lshl_add_u64 v[132:133], v[132:133], 0, s[6:7]
	global_load_dword v126, v[132:133], off
	v_lshl_add_u64 v[132:133], v[132:133], 0, s[6:7]
	global_load_dword v127, v[132:133], off
	v_lshl_add_u64 v[132:133], v[132:133], 0, s[6:7]
	global_load_dword v128, v[132:133], off
	v_lshl_add_u64 v[132:133], v[132:133], 0, s[6:7]
	global_load_dword v129, v[132:133], off
	v_lshl_add_u64 v[132:133], v[132:133], 0, s[6:7]
	global_load_dword v130, v[132:133], off
	v_lshl_add_u64 v[132:133], v[132:133], 0, s[6:7]
	global_load_dword v131, v[132:133], off
	s_waitcnt vmcnt(31)
	v_mul_f32_e32 v7, 0xbfb8aa3b, v100
	v_exp_f32_e32 v7, v7
	s_nop 0
	v_add_f32_e32 v7, 1.0, v7
	v_div_scale_f32 v8, s[10:11], v7, v7, v100
	v_rcp_f32_e32 v9, v8
	v_div_scale_f32 v10, vcc, v100, v7, v100
	v_fma_f32 v11, -v8, v9, 1.0
	v_fmac_f32_e32 v9, v11, v9
	v_mul_f32_e32 v11, v10, v9
	v_fma_f32 v12, -v8, v11, v10
	v_fmac_f32_e32 v11, v12, v9
	v_fma_f32 v8, -v8, v11, v10
	v_div_fmas_f32 v8, v8, v9, v11
	v_div_fixup_f32 v5, v8, v7, v100
	ds_write_b32 v1, v5 offset:0
	s_waitcnt vmcnt(30)
	v_mul_f32_e32 v7, 0xbfb8aa3b, v101
	v_exp_f32_e32 v7, v7
	s_nop 0
	v_add_f32_e32 v7, 1.0, v7
	v_div_scale_f32 v8, s[10:11], v7, v7, v101
	v_rcp_f32_e32 v9, v8
	v_div_scale_f32 v10, vcc, v101, v7, v101
	v_fma_f32 v11, -v8, v9, 1.0
	v_fmac_f32_e32 v9, v11, v9
	v_mul_f32_e32 v11, v10, v9
	v_fma_f32 v12, -v8, v11, v10
	v_fmac_f32_e32 v11, v12, v9
	v_fma_f32 v8, -v8, v11, v10
	v_div_fmas_f32 v8, v8, v9, v11
	v_div_fixup_f32 v5, v8, v7, v101
	ds_write_b32 v1, v5 offset:16384
	s_waitcnt vmcnt(29)
	v_mul_f32_e32 v7, 0xbfb8aa3b, v102
	v_exp_f32_e32 v7, v7
	s_nop 0
	v_add_f32_e32 v7, 1.0, v7
	v_div_scale_f32 v8, s[10:11], v7, v7, v102
	v_rcp_f32_e32 v9, v8
	v_div_scale_f32 v10, vcc, v102, v7, v102
	v_fma_f32 v11, -v8, v9, 1.0
	v_fmac_f32_e32 v9, v11, v9
	v_mul_f32_e32 v11, v10, v9
	v_fma_f32 v12, -v8, v11, v10
	v_fmac_f32_e32 v11, v12, v9
	v_fma_f32 v8, -v8, v11, v10
	v_div_fmas_f32 v8, v8, v9, v11
	v_div_fixup_f32 v5, v8, v7, v102
	ds_write_b32 v1, v5 offset:32768
	s_waitcnt vmcnt(28)
	v_mul_f32_e32 v7, 0xbfb8aa3b, v103
	v_exp_f32_e32 v7, v7
	s_nop 0
	v_add_f32_e32 v7, 1.0, v7
	v_div_scale_f32 v8, s[10:11], v7, v7, v103
	v_rcp_f32_e32 v9, v8
	v_div_scale_f32 v10, vcc, v103, v7, v103
	v_fma_f32 v11, -v8, v9, 1.0
	v_fmac_f32_e32 v9, v11, v9
	v_mul_f32_e32 v11, v10, v9
	v_fma_f32 v12, -v8, v11, v10
	v_fmac_f32_e32 v11, v12, v9
	v_fma_f32 v8, -v8, v11, v10
	v_div_fmas_f32 v8, v8, v9, v11
	v_div_fixup_f32 v5, v8, v7, v103
	ds_write_b32 v1, v5 offset:49152
	s_waitcnt vmcnt(27)
	v_mul_f32_e32 v7, 0xbfb8aa3b, v104
	v_exp_f32_e32 v7, v7
	s_nop 0
	v_add_f32_e32 v7, 1.0, v7
	v_div_scale_f32 v8, s[10:11], v7, v7, v104
	v_rcp_f32_e32 v9, v8
	v_div_scale_f32 v10, vcc, v104, v7, v104
	v_fma_f32 v11, -v8, v9, 1.0
	v_fmac_f32_e32 v9, v11, v9
	v_mul_f32_e32 v11, v10, v9
	v_fma_f32 v12, -v8, v11, v10
	v_fmac_f32_e32 v11, v12, v9
	v_fma_f32 v8, -v8, v11, v10
	v_div_fmas_f32 v8, v8, v9, v11
	v_div_fixup_f32 v5, v8, v7, v104
	ds_write_b32 v1, v5 offset:4
	s_waitcnt vmcnt(26)
	v_mul_f32_e32 v7, 0xbfb8aa3b, v105
	v_exp_f32_e32 v7, v7
	s_nop 0
	v_add_f32_e32 v7, 1.0, v7
	v_div_scale_f32 v8, s[10:11], v7, v7, v105
	v_rcp_f32_e32 v9, v8
	v_div_scale_f32 v10, vcc, v105, v7, v105
	v_fma_f32 v11, -v8, v9, 1.0
	v_fmac_f32_e32 v9, v11, v9
	v_mul_f32_e32 v11, v10, v9
	v_fma_f32 v12, -v8, v11, v10
	v_fmac_f32_e32 v11, v12, v9
	v_fma_f32 v8, -v8, v11, v10
	v_div_fmas_f32 v8, v8, v9, v11
	v_div_fixup_f32 v5, v8, v7, v105
	ds_write_b32 v1, v5 offset:16388
	s_waitcnt vmcnt(25)
	v_mul_f32_e32 v7, 0xbfb8aa3b, v106
	v_exp_f32_e32 v7, v7
	s_nop 0
	v_add_f32_e32 v7, 1.0, v7
	v_div_scale_f32 v8, s[10:11], v7, v7, v106
	v_rcp_f32_e32 v9, v8
	v_div_scale_f32 v10, vcc, v106, v7, v106
	v_fma_f32 v11, -v8, v9, 1.0
	v_fmac_f32_e32 v9, v11, v9
	v_mul_f32_e32 v11, v10, v9
	v_fma_f32 v12, -v8, v11, v10
	v_fmac_f32_e32 v11, v12, v9
	v_fma_f32 v8, -v8, v11, v10
	v_div_fmas_f32 v8, v8, v9, v11
	v_div_fixup_f32 v5, v8, v7, v106
	ds_write_b32 v1, v5 offset:32772
	s_waitcnt vmcnt(24)
	v_mul_f32_e32 v7, 0xbfb8aa3b, v107
	v_exp_f32_e32 v7, v7
	s_nop 0
	v_add_f32_e32 v7, 1.0, v7
	v_div_scale_f32 v8, s[10:11], v7, v7, v107
	v_rcp_f32_e32 v9, v8
	v_div_scale_f32 v10, vcc, v107, v7, v107
	v_fma_f32 v11, -v8, v9, 1.0
	v_fmac_f32_e32 v9, v11, v9
	v_mul_f32_e32 v11, v10, v9
	v_fma_f32 v12, -v8, v11, v10
	v_fmac_f32_e32 v11, v12, v9
	v_fma_f32 v8, -v8, v11, v10
	v_div_fmas_f32 v8, v8, v9, v11
	v_div_fixup_f32 v5, v8, v7, v107
	ds_write_b32 v1, v5 offset:49156
	s_waitcnt vmcnt(23)
	v_mul_f32_e32 v7, 0xbfb8aa3b, v108
	v_exp_f32_e32 v7, v7
	s_nop 0
	v_add_f32_e32 v7, 1.0, v7
	v_div_scale_f32 v8, s[10:11], v7, v7, v108
	v_rcp_f32_e32 v9, v8
	v_div_scale_f32 v10, vcc, v108, v7, v108
	v_fma_f32 v11, -v8, v9, 1.0
	v_fmac_f32_e32 v9, v11, v9
	v_mul_f32_e32 v11, v10, v9
	v_fma_f32 v12, -v8, v11, v10
	v_fmac_f32_e32 v11, v12, v9
	v_fma_f32 v8, -v8, v11, v10
	v_div_fmas_f32 v8, v8, v9, v11
	v_div_fixup_f32 v5, v8, v7, v108
	ds_write_b32 v1, v5 offset:8
	s_waitcnt vmcnt(22)
	v_mul_f32_e32 v7, 0xbfb8aa3b, v109
	v_exp_f32_e32 v7, v7
	s_nop 0
	v_add_f32_e32 v7, 1.0, v7
	v_div_scale_f32 v8, s[10:11], v7, v7, v109
	v_rcp_f32_e32 v9, v8
	v_div_scale_f32 v10, vcc, v109, v7, v109
	v_fma_f32 v11, -v8, v9, 1.0
	v_fmac_f32_e32 v9, v11, v9
	v_mul_f32_e32 v11, v10, v9
	v_fma_f32 v12, -v8, v11, v10
	v_fmac_f32_e32 v11, v12, v9
	v_fma_f32 v8, -v8, v11, v10
	v_div_fmas_f32 v8, v8, v9, v11
	v_div_fixup_f32 v5, v8, v7, v109
	ds_write_b32 v1, v5 offset:16392
	s_waitcnt vmcnt(21)
	v_mul_f32_e32 v7, 0xbfb8aa3b, v110
	v_exp_f32_e32 v7, v7
	s_nop 0
	v_add_f32_e32 v7, 1.0, v7
	v_div_scale_f32 v8, s[10:11], v7, v7, v110
	v_rcp_f32_e32 v9, v8
	v_div_scale_f32 v10, vcc, v110, v7, v110
	v_fma_f32 v11, -v8, v9, 1.0
	v_fmac_f32_e32 v9, v11, v9
	v_mul_f32_e32 v11, v10, v9
	v_fma_f32 v12, -v8, v11, v10
	v_fmac_f32_e32 v11, v12, v9
	v_fma_f32 v8, -v8, v11, v10
	v_div_fmas_f32 v8, v8, v9, v11
	v_div_fixup_f32 v5, v8, v7, v110
	ds_write_b32 v1, v5 offset:32776
	s_waitcnt vmcnt(20)
	v_mul_f32_e32 v7, 0xbfb8aa3b, v111
	v_exp_f32_e32 v7, v7
	s_nop 0
	v_add_f32_e32 v7, 1.0, v7
	v_div_scale_f32 v8, s[10:11], v7, v7, v111
	v_rcp_f32_e32 v9, v8
	v_div_scale_f32 v10, vcc, v111, v7, v111
	v_fma_f32 v11, -v8, v9, 1.0
	v_fmac_f32_e32 v9, v11, v9
	v_mul_f32_e32 v11, v10, v9
	v_fma_f32 v12, -v8, v11, v10
	v_fmac_f32_e32 v11, v12, v9
	v_fma_f32 v8, -v8, v11, v10
	v_div_fmas_f32 v8, v8, v9, v11
	v_div_fixup_f32 v5, v8, v7, v111
	ds_write_b32 v1, v5 offset:49160
	s_waitcnt vmcnt(19)
	v_mul_f32_e32 v7, 0xbfb8aa3b, v112
	v_exp_f32_e32 v7, v7
	s_nop 0
	v_add_f32_e32 v7, 1.0, v7
	v_div_scale_f32 v8, s[10:11], v7, v7, v112
	v_rcp_f32_e32 v9, v8
	v_div_scale_f32 v10, vcc, v112, v7, v112
	v_fma_f32 v11, -v8, v9, 1.0
	v_fmac_f32_e32 v9, v11, v9
	v_mul_f32_e32 v11, v10, v9
	v_fma_f32 v12, -v8, v11, v10
	v_fmac_f32_e32 v11, v12, v9
	v_fma_f32 v8, -v8, v11, v10
	v_div_fmas_f32 v8, v8, v9, v11
	v_div_fixup_f32 v5, v8, v7, v112
	ds_write_b32 v1, v5 offset:12
	s_waitcnt vmcnt(18)
	v_mul_f32_e32 v7, 0xbfb8aa3b, v113
	v_exp_f32_e32 v7, v7
	s_nop 0
	v_add_f32_e32 v7, 1.0, v7
	v_div_scale_f32 v8, s[10:11], v7, v7, v113
	v_rcp_f32_e32 v9, v8
	v_div_scale_f32 v10, vcc, v113, v7, v113
	v_fma_f32 v11, -v8, v9, 1.0
	v_fmac_f32_e32 v9, v11, v9
	v_mul_f32_e32 v11, v10, v9
	v_fma_f32 v12, -v8, v11, v10
	v_fmac_f32_e32 v11, v12, v9
	v_fma_f32 v8, -v8, v11, v10
	v_div_fmas_f32 v8, v8, v9, v11
	v_div_fixup_f32 v5, v8, v7, v113
	ds_write_b32 v1, v5 offset:16396
	s_waitcnt vmcnt(17)
	v_mul_f32_e32 v7, 0xbfb8aa3b, v114
	v_exp_f32_e32 v7, v7
	s_nop 0
	v_add_f32_e32 v7, 1.0, v7
	v_div_scale_f32 v8, s[10:11], v7, v7, v114
	v_rcp_f32_e32 v9, v8
	v_div_scale_f32 v10, vcc, v114, v7, v114
	v_fma_f32 v11, -v8, v9, 1.0
	v_fmac_f32_e32 v9, v11, v9
	v_mul_f32_e32 v11, v10, v9
	v_fma_f32 v12, -v8, v11, v10
	v_fmac_f32_e32 v11, v12, v9
	v_fma_f32 v8, -v8, v11, v10
	v_div_fmas_f32 v8, v8, v9, v11
	v_div_fixup_f32 v5, v8, v7, v114
	ds_write_b32 v1, v5 offset:32780
	s_waitcnt vmcnt(16)
	v_mul_f32_e32 v7, 0xbfb8aa3b, v115
	v_exp_f32_e32 v7, v7
	s_nop 0
	v_add_f32_e32 v7, 1.0, v7
	v_div_scale_f32 v8, s[10:11], v7, v7, v115
	v_rcp_f32_e32 v9, v8
	v_div_scale_f32 v10, vcc, v115, v7, v115
	v_fma_f32 v11, -v8, v9, 1.0
	v_fmac_f32_e32 v9, v11, v9
	v_mul_f32_e32 v11, v10, v9
	v_fma_f32 v12, -v8, v11, v10
	v_fmac_f32_e32 v11, v12, v9
	v_fma_f32 v8, -v8, v11, v10
	v_div_fmas_f32 v8, v8, v9, v11
	v_div_fixup_f32 v5, v8, v7, v115
	ds_write_b32 v1, v5 offset:49164
	s_waitcnt vmcnt(15)
	v_mul_f32_e32 v7, 0xbfb8aa3b, v116
	v_exp_f32_e32 v7, v7
	s_nop 0
	v_add_f32_e32 v7, 1.0, v7
	v_div_scale_f32 v8, s[10:11], v7, v7, v116
	v_rcp_f32_e32 v9, v8
	v_div_scale_f32 v10, vcc, v116, v7, v116
	v_fma_f32 v11, -v8, v9, 1.0
	v_fmac_f32_e32 v9, v11, v9
	v_mul_f32_e32 v11, v10, v9
	v_fma_f32 v12, -v8, v11, v10
	v_fmac_f32_e32 v11, v12, v9
	v_fma_f32 v8, -v8, v11, v10
	v_div_fmas_f32 v8, v8, v9, v11
	v_div_fixup_f32 v5, v8, v7, v116
	ds_write_b32 v1, v5 offset:16
	s_waitcnt vmcnt(14)
	v_mul_f32_e32 v7, 0xbfb8aa3b, v117
	v_exp_f32_e32 v7, v7
	s_nop 0
	v_add_f32_e32 v7, 1.0, v7
	v_div_scale_f32 v8, s[10:11], v7, v7, v117
	v_rcp_f32_e32 v9, v8
	v_div_scale_f32 v10, vcc, v117, v7, v117
	v_fma_f32 v11, -v8, v9, 1.0
	v_fmac_f32_e32 v9, v11, v9
	v_mul_f32_e32 v11, v10, v9
	v_fma_f32 v12, -v8, v11, v10
	v_fmac_f32_e32 v11, v12, v9
	v_fma_f32 v8, -v8, v11, v10
	v_div_fmas_f32 v8, v8, v9, v11
	v_div_fixup_f32 v5, v8, v7, v117
	ds_write_b32 v1, v5 offset:16400
	s_waitcnt vmcnt(13)
	v_mul_f32_e32 v7, 0xbfb8aa3b, v118
	v_exp_f32_e32 v7, v7
	s_nop 0
	v_add_f32_e32 v7, 1.0, v7
	v_div_scale_f32 v8, s[10:11], v7, v7, v118
	v_rcp_f32_e32 v9, v8
	v_div_scale_f32 v10, vcc, v118, v7, v118
	v_fma_f32 v11, -v8, v9, 1.0
	v_fmac_f32_e32 v9, v11, v9
	v_mul_f32_e32 v11, v10, v9
	v_fma_f32 v12, -v8, v11, v10
	v_fmac_f32_e32 v11, v12, v9
	v_fma_f32 v8, -v8, v11, v10
	v_div_fmas_f32 v8, v8, v9, v11
	v_div_fixup_f32 v5, v8, v7, v118
	ds_write_b32 v1, v5 offset:32784
	s_waitcnt vmcnt(12)
	v_mul_f32_e32 v7, 0xbfb8aa3b, v119
	v_exp_f32_e32 v7, v7
	s_nop 0
	v_add_f32_e32 v7, 1.0, v7
	v_div_scale_f32 v8, s[10:11], v7, v7, v119
	v_rcp_f32_e32 v9, v8
	v_div_scale_f32 v10, vcc, v119, v7, v119
	v_fma_f32 v11, -v8, v9, 1.0
	v_fmac_f32_e32 v9, v11, v9
	v_mul_f32_e32 v11, v10, v9
	v_fma_f32 v12, -v8, v11, v10
	v_fmac_f32_e32 v11, v12, v9
	v_fma_f32 v8, -v8, v11, v10
	v_div_fmas_f32 v8, v8, v9, v11
	v_div_fixup_f32 v5, v8, v7, v119
	ds_write_b32 v1, v5 offset:49168
	s_waitcnt vmcnt(11)
	v_mul_f32_e32 v7, 0xbfb8aa3b, v120
	v_exp_f32_e32 v7, v7
	s_nop 0
	v_add_f32_e32 v7, 1.0, v7
	v_div_scale_f32 v8, s[10:11], v7, v7, v120
	v_rcp_f32_e32 v9, v8
	v_div_scale_f32 v10, vcc, v120, v7, v120
	v_fma_f32 v11, -v8, v9, 1.0
	v_fmac_f32_e32 v9, v11, v9
	v_mul_f32_e32 v11, v10, v9
	v_fma_f32 v12, -v8, v11, v10
	v_fmac_f32_e32 v11, v12, v9
	v_fma_f32 v8, -v8, v11, v10
	v_div_fmas_f32 v8, v8, v9, v11
	v_div_fixup_f32 v5, v8, v7, v120
	ds_write_b32 v1, v5 offset:20
	s_waitcnt vmcnt(10)
	v_mul_f32_e32 v7, 0xbfb8aa3b, v121
	v_exp_f32_e32 v7, v7
	s_nop 0
	v_add_f32_e32 v7, 1.0, v7
	v_div_scale_f32 v8, s[10:11], v7, v7, v121
	v_rcp_f32_e32 v9, v8
	v_div_scale_f32 v10, vcc, v121, v7, v121
	v_fma_f32 v11, -v8, v9, 1.0
	v_fmac_f32_e32 v9, v11, v9
	v_mul_f32_e32 v11, v10, v9
	v_fma_f32 v12, -v8, v11, v10
	v_fmac_f32_e32 v11, v12, v9
	v_fma_f32 v8, -v8, v11, v10
	v_div_fmas_f32 v8, v8, v9, v11
	v_div_fixup_f32 v5, v8, v7, v121
	ds_write_b32 v1, v5 offset:16404
	s_waitcnt vmcnt(9)
	v_mul_f32_e32 v7, 0xbfb8aa3b, v122
	v_exp_f32_e32 v7, v7
	s_nop 0
	v_add_f32_e32 v7, 1.0, v7
	v_div_scale_f32 v8, s[10:11], v7, v7, v122
	v_rcp_f32_e32 v9, v8
	v_div_scale_f32 v10, vcc, v122, v7, v122
	v_fma_f32 v11, -v8, v9, 1.0
	v_fmac_f32_e32 v9, v11, v9
	v_mul_f32_e32 v11, v10, v9
	v_fma_f32 v12, -v8, v11, v10
	v_fmac_f32_e32 v11, v12, v9
	v_fma_f32 v8, -v8, v11, v10
	v_div_fmas_f32 v8, v8, v9, v11
	v_div_fixup_f32 v5, v8, v7, v122
	ds_write_b32 v1, v5 offset:32788
	s_waitcnt vmcnt(8)
	v_mul_f32_e32 v7, 0xbfb8aa3b, v123
	v_exp_f32_e32 v7, v7
	s_nop 0
	v_add_f32_e32 v7, 1.0, v7
	v_div_scale_f32 v8, s[10:11], v7, v7, v123
	v_rcp_f32_e32 v9, v8
	v_div_scale_f32 v10, vcc, v123, v7, v123
	v_fma_f32 v11, -v8, v9, 1.0
	v_fmac_f32_e32 v9, v11, v9
	v_mul_f32_e32 v11, v10, v9
	v_fma_f32 v12, -v8, v11, v10
	v_fmac_f32_e32 v11, v12, v9
	v_fma_f32 v8, -v8, v11, v10
	v_div_fmas_f32 v8, v8, v9, v11
	v_div_fixup_f32 v5, v8, v7, v123
	ds_write_b32 v1, v5 offset:49172
	s_waitcnt vmcnt(7)
	v_mul_f32_e32 v7, 0xbfb8aa3b, v124
	v_exp_f32_e32 v7, v7
	s_nop 0
	v_add_f32_e32 v7, 1.0, v7
	v_div_scale_f32 v8, s[10:11], v7, v7, v124
	v_rcp_f32_e32 v9, v8
	v_div_scale_f32 v10, vcc, v124, v7, v124
	v_fma_f32 v11, -v8, v9, 1.0
	v_fmac_f32_e32 v9, v11, v9
	v_mul_f32_e32 v11, v10, v9
	v_fma_f32 v12, -v8, v11, v10
	v_fmac_f32_e32 v11, v12, v9
	v_fma_f32 v8, -v8, v11, v10
	v_div_fmas_f32 v8, v8, v9, v11
	v_div_fixup_f32 v5, v8, v7, v124
	ds_write_b32 v1, v5 offset:24
	s_waitcnt vmcnt(6)
	v_mul_f32_e32 v7, 0xbfb8aa3b, v125
	v_exp_f32_e32 v7, v7
	s_nop 0
	v_add_f32_e32 v7, 1.0, v7
	v_div_scale_f32 v8, s[10:11], v7, v7, v125
	v_rcp_f32_e32 v9, v8
	v_div_scale_f32 v10, vcc, v125, v7, v125
	v_fma_f32 v11, -v8, v9, 1.0
	v_fmac_f32_e32 v9, v11, v9
	v_mul_f32_e32 v11, v10, v9
	v_fma_f32 v12, -v8, v11, v10
	v_fmac_f32_e32 v11, v12, v9
	v_fma_f32 v8, -v8, v11, v10
	v_div_fmas_f32 v8, v8, v9, v11
	v_div_fixup_f32 v5, v8, v7, v125
	ds_write_b32 v1, v5 offset:16408
	s_waitcnt vmcnt(5)
	v_mul_f32_e32 v7, 0xbfb8aa3b, v126
	v_exp_f32_e32 v7, v7
	s_nop 0
	v_add_f32_e32 v7, 1.0, v7
	v_div_scale_f32 v8, s[10:11], v7, v7, v126
	v_rcp_f32_e32 v9, v8
	v_div_scale_f32 v10, vcc, v126, v7, v126
	v_fma_f32 v11, -v8, v9, 1.0
	v_fmac_f32_e32 v9, v11, v9
	v_mul_f32_e32 v11, v10, v9
	v_fma_f32 v12, -v8, v11, v10
	v_fmac_f32_e32 v11, v12, v9
	v_fma_f32 v8, -v8, v11, v10
	v_div_fmas_f32 v8, v8, v9, v11
	v_div_fixup_f32 v5, v8, v7, v126
	ds_write_b32 v1, v5 offset:32792
	s_waitcnt vmcnt(4)
	v_mul_f32_e32 v7, 0xbfb8aa3b, v127
	v_exp_f32_e32 v7, v7
	s_nop 0
	v_add_f32_e32 v7, 1.0, v7
	v_div_scale_f32 v8, s[10:11], v7, v7, v127
	v_rcp_f32_e32 v9, v8
	v_div_scale_f32 v10, vcc, v127, v7, v127
	v_fma_f32 v11, -v8, v9, 1.0
	v_fmac_f32_e32 v9, v11, v9
	v_mul_f32_e32 v11, v10, v9
	v_fma_f32 v12, -v8, v11, v10
	v_fmac_f32_e32 v11, v12, v9
	v_fma_f32 v8, -v8, v11, v10
	v_div_fmas_f32 v8, v8, v9, v11
	v_div_fixup_f32 v5, v8, v7, v127
	ds_write_b32 v1, v5 offset:49176
	s_waitcnt vmcnt(3)
	v_mul_f32_e32 v7, 0xbfb8aa3b, v128
	v_exp_f32_e32 v7, v7
	s_nop 0
	v_add_f32_e32 v7, 1.0, v7
	v_div_scale_f32 v8, s[10:11], v7, v7, v128
	v_rcp_f32_e32 v9, v8
	v_div_scale_f32 v10, vcc, v128, v7, v128
	v_fma_f32 v11, -v8, v9, 1.0
	v_fmac_f32_e32 v9, v11, v9
	v_mul_f32_e32 v11, v10, v9
	v_fma_f32 v12, -v8, v11, v10
	v_fmac_f32_e32 v11, v12, v9
	v_fma_f32 v8, -v8, v11, v10
	v_div_fmas_f32 v8, v8, v9, v11
	v_div_fixup_f32 v5, v8, v7, v128
	ds_write_b32 v1, v5 offset:28
	s_waitcnt vmcnt(2)
	v_mul_f32_e32 v7, 0xbfb8aa3b, v129
	v_exp_f32_e32 v7, v7
	s_nop 0
	v_add_f32_e32 v7, 1.0, v7
	v_div_scale_f32 v8, s[10:11], v7, v7, v129
	v_rcp_f32_e32 v9, v8
	v_div_scale_f32 v10, vcc, v129, v7, v129
	v_fma_f32 v11, -v8, v9, 1.0
	v_fmac_f32_e32 v9, v11, v9
	v_mul_f32_e32 v11, v10, v9
	v_fma_f32 v12, -v8, v11, v10
	v_fmac_f32_e32 v11, v12, v9
	v_fma_f32 v8, -v8, v11, v10
	v_div_fmas_f32 v8, v8, v9, v11
	v_div_fixup_f32 v5, v8, v7, v129
	ds_write_b32 v1, v5 offset:16412
	s_waitcnt vmcnt(1)
	v_mul_f32_e32 v7, 0xbfb8aa3b, v130
	v_exp_f32_e32 v7, v7
	s_nop 0
	v_add_f32_e32 v7, 1.0, v7
	v_div_scale_f32 v8, s[10:11], v7, v7, v130
	v_rcp_f32_e32 v9, v8
	v_div_scale_f32 v10, vcc, v130, v7, v130
	v_fma_f32 v11, -v8, v9, 1.0
	v_fmac_f32_e32 v9, v11, v9
	v_mul_f32_e32 v11, v10, v9
	v_fma_f32 v12, -v8, v11, v10
	v_fmac_f32_e32 v11, v12, v9
	v_fma_f32 v8, -v8, v11, v10
	v_div_fmas_f32 v8, v8, v9, v11
	v_div_fixup_f32 v5, v8, v7, v130
	ds_write_b32 v1, v5 offset:32796
	s_waitcnt vmcnt(0)
	v_mul_f32_e32 v7, 0xbfb8aa3b, v131
	v_exp_f32_e32 v7, v7
	s_nop 0
	v_add_f32_e32 v7, 1.0, v7
	v_div_scale_f32 v8, s[10:11], v7, v7, v131
	v_rcp_f32_e32 v9, v8
	v_div_scale_f32 v10, vcc, v131, v7, v131
	v_fma_f32 v11, -v8, v9, 1.0
	v_fmac_f32_e32 v9, v11, v9
	v_mul_f32_e32 v11, v10, v9
	v_fma_f32 v12, -v8, v11, v10
	v_fmac_f32_e32 v11, v12, v9
	v_fma_f32 v8, -v8, v11, v10
	v_div_fmas_f32 v8, v8, v9, v11
	v_div_fixup_f32 v5, v8, v7, v131
	ds_write_b32 v1, v5 offset:49180

.LBB0_2639:
	s_cmp_lt_i32 s56, 12
	s_cselect_b64 s[0:1], -1, 0
	s_cmp_gt_i32 s57, 11
	s_cselect_b64 s[2:3], -1, 0
	s_and_b64 s[0:1], s[0:1], s[2:3]
	s_andn2_b64 vcc, exec, s[0:1]
	s_cbranch_vccnz .LBB0_3508
	s_and_b32 s0, s86, 7
	s_mul_i32 s0, s0, 3
	s_mov_b32 s0, 0
	s_add_u32 s1, s96, 0x3ea00000
	v_writelane_b32 v255, s1, 11
	s_addc_u32 s1, s97, 0
	v_writelane_b32 v255, s1, 12
	s_add_u32 s1, s96, 0x4aa00000
	v_readlane_b32 s4, v254, 7
	v_writelane_b32 v255, s1, 13
	s_addc_u32 s1, s97, 0
	s_ashr_i32 s3, s4, 31
	s_mul_i32 s2, s94, s0
	v_writelane_b32 v255, s1, 14
	s_mul_hi_i32 s1, s94, s0
	s_add_u32 s0, s2, s4
	s_addc_u32 s1, s1, s3
	s_waitcnt vmcnt(0)
	v_mov_b64_e32 v[2:3], 0x200
	v_mov_b32_e32 v1, v0
	v_writelane_b32 v255, s2, 15
	v_cmp_lt_i64_e32 vcc, s[0:1], v[2:3]
	v_writelane_b32 v255, s3, 16
	s_and_b64 s[2:3], vcc, exec
	s_cselect_b32 s0, s0, 0x200
	v_bfe_u32 v1, v0, 5, 1
	v_writelane_b32 v255, s0, 17
	s_cmp_ge_i32 s4, s0
	v_and_b32_e32 v182, 31, v0
	v_lshlrev_b32_e32 v199, 3, v0
	v_and_b32_e32 v196, 63, v0
	v_lshlrev_b32_e32 v185, 2, v1
	v_lshlrev_b32_e32 v184, 3, v1
	v_lshlrev_b32_e32 v198, 4, v1
	v_and_b32_e32 v197, 3, v0
	v_lshlrev_b32_e32 v186, 13, v1
	s_cbranch_scc1 .LBB0_2890
	v_readlane_b32 s74, v254, 7
	s_ashr_i32 s2, s74, 6
	s_ashr_i32 s3, s2, 31
	s_lshl_b32 s1, s74, 8
	s_lshl_b64 s[4:5], s[2:3], 11
	s_and_b32 s24, s1, 0x300
	s_or_b32 s4, s4, s24
	s_mul_i32 s1, s5, 0x3000
	s_mul_hi_u32 s3, s4, 0x3000
	s_ashr_i32 s0, s74, 2
	s_add_i32 s3, s3, s1
	s_mul_i32 s1, s4, 0x3000
	v_readlane_b32 s8, v255, 11
	s_add_u32 s1, s8, s1
	v_readlane_b32 s9, v255, 12
	s_addc_u32 s3, s9, s3
	s_lshl_b32 s6, s0, 7
	s_and_b32 s6, s6, 0x780
	s_lshl_b32 s7, s6, 1
	s_add_u32 s10, s1, s7
	s_addc_u32 s11, s3, 0
	s_mul_hi_i32 s1, s2, 0x1800000
	s_mul_i32 s2, s2, 0x1800000
	s_add_u32 s2, s8, s2
	s_addc_u32 s1, s9, s1
	s_add_u32 s2, s2, s7
	s_addc_u32 s1, s1, 0
	s_add_u32 s70, s2, 0x1000
	s_addc_u32 s71, s1, 0
	s_add_u32 s90, s2, 0x2000
	s_addc_u32 s91, s1, 0
	s_lshl_b64 s[2:3], s[4:5], 11
	v_readlane_b32 s1, v255, 13
	s_add_u32 s1, s1, s2
	v_readlane_b32 s2, v255, 14
	s_addc_u32 s2, s2, s3
	s_add_u32 s88, s1, s6
	s_addc_u32 s89, s2, 0
	s_ashr_i32 s1, s0, 31
	s_lshl_b64 s[0:1], s[0:1], 12
	v_readlane_b32 s2, v255, 7
	v_readlane_b32 s3, v255, 8
	s_add_u32 s8, s2, s0
	v_readfirstlane_b32 s0, v0
	s_addc_u32 s9, s3, s1
	s_lshr_b32 s2, s0, 6
	s_movk_i32 s33, 0x3000
	v_lshl_or_b32 v1, s2, 5, v182
	v_writelane_b32 v255, s10, 18
	v_and_b32_e32 v20, 0x78, v199
	v_lshlrev_b32_e32 v22, 1, v20
	v_mov_b64_e32 v[2:3], s[10:11]
	v_mad_u64_u32 v[4:5], s[0:1], v1, s33, v[2:3]
	v_or_b32_e32 v1, s24, v227
	v_and_b32_e32 v2, 16, v226
	v_mov_b32_e32 v3, 0
	v_mul_u32_u24_e32 v1, 0x1800, v1
	v_lshl_add_u64 v[4:5], v[4:5], 0, v[2:3]
	v_lshlrev_b32_e32 v2, 1, v1
	v_or_b32_e32 v1, 32, v227
	v_or_b32_e32 v6, s24, v1
	v_mul_u32_u24_e32 v6, 0x1800, v6
	v_mov_b32_e32 v23, v3
	v_lshlrev_b32_e32 v6, 1, v6
	v_mov_b32_e32 v7, v3
	v_lshl_add_u64 v[8:9], s[70:71], 0, v[2:3]
	v_lshl_add_u64 v[8:9], v[8:9], 0, v[22:23]
	v_lshl_add_u64 v[10:11], s[70:71], 0, v[6:7]
	v_lshl_add_u64 v[10:11], v[10:11], 0, v[22:23]
	global_load_dwordx4 v[12:15], v[8:9], off
	global_load_dwordx4 v[16:19], v[10:11], off
	s_lshl_b32 s0, s2, 13
	s_add_i32 s0, s0, 0
	s_add_i32 m0, s0, 0x10840
	v_lshl_add_u64 v[8:9], v[4:5], 0, 32
	global_load_lds_dwordx4 v[4:5], off
	s_add_i32 m0, s0, 0x10c40
	s_mov_b64 s[2:3], 0x60
	global_load_lds_dwordx4 v[8:9], off
	v_lshl_add_u64 v[8:9], v[4:5], 0, 64
	s_add_i32 m0, s0, 0x11040
	v_lshl_add_u64 v[6:7], s[90:91], 0, v[6:7]
	global_load_lds_dwordx4 v[8:9], off
	v_lshl_add_u64 v[8:9], v[4:5], 0, s[2:3]
	s_add_i32 m0, s0, 0x11440
	s_mov_b64 s[2:3], 0x80
	global_load_lds_dwordx4 v[8:9], off
	v_lshl_add_u64 v[8:9], v[4:5], 0, s[2:3]
	s_add_i32 m0, s0, 0x11840
	s_mov_b64 s[2:3], 0xa0
	global_load_lds_dwordx4 v[8:9], off
	v_lshl_add_u64 v[8:9], v[4:5], 0, s[2:3]
	s_add_i32 m0, s0, 0x11c40
	s_mov_b64 s[2:3], 0xc0
	global_load_lds_dwordx4 v[8:9], off
	v_lshl_add_u64 v[8:9], v[4:5], 0, s[2:3]
	s_add_i32 m0, s0, 0x12040
	s_mov_b64 s[2:3], 0xe0
	global_load_lds_dwordx4 v[8:9], off
	v_lshl_add_u64 v[4:5], v[4:5], 0, s[2:3]
	s_add_i32 m0, s0, 0x12440
	v_lshl_add_u64 v[8:9], v[6:7], 0, v[22:23]
	global_load_lds_dwordx4 v[4:5], off
	v_lshl_add_u64 v[4:5], s[90:91], 0, v[2:3]
	v_lshl_add_u64 v[4:5], v[4:5], 0, v[22:23]
	global_load_dwordx4 v[4:7], v[4:5], off
	s_nop 0
	global_load_dwordx4 v[8:11], v[8:9], off
	s_movk_i32 s0, 0x70
	v_lshlrev_b32_e32 v2, 8, v227
	v_bitop3_b32 v23, v22, v0, s0 bitop3:0x78
	v_add3_u32 v23, 0, v2, v23
	s_waitcnt vmcnt(0)
	s_waitcnt vmcnt(0)
	ds_write_b128 v23, v[12:15] offset:32768
	ds_write_b128 v23, v[16:19] offset:40960
	v_lshrrev_b32_e32 v12, 3, v0
	v_and_b32_e32 v12, 8, v12
	v_and_or_b32 v13, v227, 16, v12
	v_and_or_b32 v12, v1, 48, v12
	v_lshrrev_b32_e32 v13, 1, v13
	v_bfe_u32 v14, v199, 5, 2
	v_lshrrev_b32_e32 v15, 5, v0
	v_lshrrev_b32_e32 v12, 1, v12
	v_or_b32_e32 v13, v13, v14
	v_and_or_b32 v15, v15, 4, v223
	v_or_b32_e32 v12, v12, v14
	v_writelane_b32 v255, s11, 19
	v_lshlrev_b32_e32 v13, 9, v13
	v_lshlrev_b32_e32 v15, 6, v15
	v_and_b32_e32 v16, 48, v22
	v_lshlrev_b32_e32 v12, 9, v12
	v_lshlrev_b32_e32 v201, 4, v196
	v_cmp_eq_u32_e64 s[2:3], 0, v196
	v_or3_b32 v13, v13, v15, v16
	v_or3_b32 v12, v12, v15, v16
	v_and_b32_e32 v14, 0xc0, v201
	v_and_b32_e32 v15, 32, v225
	v_and_b32_e32 v16, 0x118, v199
	v_writelane_b32 v255, s2, 20
	v_or3_b32 v14, v16, v15, v14
	v_bitop3_b32 v16, v198, v249, s0 bitop3:0x78
	v_writelane_b32 v255, s3, 21
	s_add_i32 s0, 0, 0x10810
	v_writelane_b32 v255, s0, 22
	v_writelane_b32 v255, s8, 23
	v_and_b32_e32 v21, 0x70, v0
	s_movk_i32 s1, 0x60
	v_writelane_b32 v255, s9, 24
	v_writelane_b32 v255, s88, 25
	v_add_u32_e32 v204, 0, v14
	v_and_b32_e32 v14, 0x70, v249
	v_writelane_b32 v255, s89, 26
	v_bitop3_b32 v2, v22, v2, v21 bitop3:0xde
	v_lshl_add_u32 v15, v182, 8, 0
	v_bitop3_b32 v17, v198, v14, 32 bitop3:0x36
	v_bitop3_b32 v19, v198, v14, 64 bitop3:0x36
	v_bitop3_b32 v14, v198, v14, s1 bitop3:0x36
	v_writelane_b32 v255, s70, 9
	s_mov_b32 s73, 0
	v_sub_u32_e32 v200, v182, v185
	v_or_b32_e32 v202, 64, v227
	v_or_b32_e32 v203, 0x60, v227
	v_cmp_gt_u32_e64 s[4:5], 32, v196
	v_cmp_eq_u32_e64 s[6:7], 0, v197
	v_mov_b32_e32 v183, v3
	v_mov_b32_e32 v187, v3
	s_mov_b32 s1, 0x41000000
	v_lshlrev_b32_e32 v188, 1, v20
	s_mov_b32 s0, 0x3e0293ee
	v_lshlrev_b32_e32 v190, 1, v184
	s_mov_b32 s92, 0xc3e00000
	v_add_u32_e32 v205, 0, v13
	v_add_u32_e32 v206, 0, v12
	v_mov_b32_e32 v18, 0xff800000
	v_add_u32_e32 v207, v15, v16
	v_add_u32_e32 v208, v15, v17
	v_add_u32_e32 v209, v15, v19
	v_add_u32_e32 v210, v15, v14
	v_add_u32_e32 v211, 0, v2
	v_mov_b32_e32 v212, 0xf149f2ca
	v_mov_b32_e32 v213, 0x43e00000
	s_mov_b32 s93, 0
	s_mov_b32 s75, s24
	s_mov_b64 s[78:79], s[90:91]
	v_writelane_b32 v255, s71, 10
	s_waitcnt lgkmcnt(0)
	s_barrier
	s_branch .LBB0_2643
